# copy shares rebalanced after conv speedup: trims L0 17,17,17 L1 30,30,25 (more copy left on classes 1/2)
# baseline (speedup 1.0000x reference)
.LBB0_1363:
.LBB0_1365:
.LBB0_1366:
.LBB0_1368:
.LBB0_1370:
.LBB0_1372:
.LBB0_1374:
.LBB0_1378:
.LBB0_1380:
.LBB0_1381:
.LBB0_1383:
.LBB0_1385:
.LBB0_1387:
.LBB0_1388:
.LBB0_1390:
.LBB0_1392:
.LBB0_1393:
.LBB0_1394:
.LBB0_1395:
.LBB0_1397:
.LBB0_1401:
.LBB0_1403:
.LBB0_1404:
.LBB0_1406:
.LBB0_1408:
.LBB0_1410:
.LBB0_1411:
.LBB0_1414:
.LBB0_1418:
.LBB0_1420:
.LBB0_1421:
.LBB0_1423:
.LBB0_1425:
.Lmoe_site_A:
	s_nop 1
	v_writelane_b32 v255, s0, 0
	v_writelane_b32 v255, s1, 1
	v_writelane_b32 v255, s2, 2
	v_writelane_b32 v255, s3, 3
	v_writelane_b32 v255, s4, 4
	v_writelane_b32 v255, s5, 5
	v_writelane_b32 v255, s6, 6
	v_writelane_b32 v255, s7, 7
	v_writelane_b32 v255, s8, 8
	v_writelane_b32 v255, s9, 9
	v_writelane_b32 v255, s10, 10
	v_writelane_b32 v255, s11, 11
	v_writelane_b32 v255, s12, 12
	v_writelane_b32 v255, s13, 13
	v_writelane_b32 v255, s14, 14
	v_writelane_b32 v255, s15, 15
	v_writelane_b32 v255, s16, 16
	v_writelane_b32 v255, s17, 17
	v_writelane_b32 v255, s18, 18
	v_writelane_b32 v255, s19, 19
	v_writelane_b32 v255, s20, 20
	v_writelane_b32 v255, s21, 21
	v_writelane_b32 v255, s22, 22
	v_writelane_b32 v255, s23, 23
	v_writelane_b32 v255, s24, 24
	v_writelane_b32 v255, s25, 25
	v_writelane_b32 v255, s26, 26
	v_writelane_b32 v255, s27, 27
	v_writelane_b32 v255, s28, 28
	v_writelane_b32 v255, s29, 29
	v_writelane_b32 v255, s30, 30
	v_writelane_b32 v255, s31, 31
	v_writelane_b32 v255, s32, 32
	v_writelane_b32 v255, s33, 33
	v_writelane_b32 v255, s34, 34
	v_writelane_b32 v255, s35, 35
	s_movk_i32 s0, 0
	s_movk_i32 s2, 16
	s_mov_b32 s4, 0x7800
	s_mov_b32 s5, 0xda00
	s_mov_b32 s34, 0xc000
	s_branch .Lmoe_p4
.Lmoe_site_B:
	s_nop 1
	v_writelane_b32 v255, s0, 0
	v_writelane_b32 v255, s1, 1
	v_writelane_b32 v255, s2, 2
	v_writelane_b32 v255, s3, 3
	v_writelane_b32 v255, s4, 4
	v_writelane_b32 v255, s5, 5
	v_writelane_b32 v255, s6, 6
	v_writelane_b32 v255, s7, 7
	v_writelane_b32 v255, s8, 8
	v_writelane_b32 v255, s9, 9
	v_writelane_b32 v255, s10, 10
	v_writelane_b32 v255, s11, 11
	v_writelane_b32 v255, s12, 12
	v_writelane_b32 v255, s13, 13
	v_writelane_b32 v255, s14, 14
	v_writelane_b32 v255, s15, 15
	v_writelane_b32 v255, s16, 16
	v_writelane_b32 v255, s17, 17
	v_writelane_b32 v255, s18, 18
	v_writelane_b32 v255, s19, 19
	v_writelane_b32 v255, s20, 20
	v_writelane_b32 v255, s21, 21
	v_writelane_b32 v255, s22, 22
	v_writelane_b32 v255, s23, 23
	v_writelane_b32 v255, s24, 24
	v_writelane_b32 v255, s25, 25
	v_writelane_b32 v255, s26, 26
	v_writelane_b32 v255, s27, 27
	v_writelane_b32 v255, s28, 28
	v_writelane_b32 v255, s29, 29
	v_writelane_b32 v255, s30, 30
	v_writelane_b32 v255, s31, 31
	v_writelane_b32 v255, s32, 32
	v_writelane_b32 v255, s33, 33
	v_writelane_b32 v255, s34, 34
	v_writelane_b32 v255, s35, 35
	s_movk_i32 s0, 1
	s_movk_i32 s2, 8
	s_mov_b32 s4, 0x800
	s_mov_b32 s5, 0x5600
	s_mov_b32 s34, 0x4600
	s_branch .Lmoe_p4

.Lmoe_site_E:
	s_nop 1
	v_writelane_b32 v255, s0, 0
	v_writelane_b32 v255, s1, 1
	v_writelane_b32 v255, s2, 2
	v_writelane_b32 v255, s3, 3
	v_writelane_b32 v255, s4, 4
	v_writelane_b32 v255, s5, 5
	v_writelane_b32 v255, s6, 6
	v_writelane_b32 v255, s7, 7
	v_writelane_b32 v255, s8, 8
	v_writelane_b32 v255, s9, 9
	v_writelane_b32 v255, s10, 10
	v_writelane_b32 v255, s11, 11
	v_writelane_b32 v255, s12, 12
	v_writelane_b32 v255, s13, 13
	v_writelane_b32 v255, s14, 14
	v_writelane_b32 v255, s15, 15
	v_writelane_b32 v255, s16, 16
	v_writelane_b32 v255, s17, 17
	v_writelane_b32 v255, s18, 18
	v_writelane_b32 v255, s19, 19
	v_writelane_b32 v255, s20, 20
	v_writelane_b32 v255, s21, 21
	v_writelane_b32 v255, s22, 22
	v_writelane_b32 v255, s23, 23
	v_writelane_b32 v255, s24, 24
	v_writelane_b32 v255, s25, 25
	v_writelane_b32 v255, s26, 26
	v_writelane_b32 v255, s27, 27
	v_writelane_b32 v255, s28, 28
	v_writelane_b32 v255, s29, 29
	v_writelane_b32 v255, s30, 30
	v_writelane_b32 v255, s31, 31
	v_writelane_b32 v255, s32, 32
	v_writelane_b32 v255, s33, 33
	v_writelane_b32 v255, s34, 34
	v_writelane_b32 v255, s35, 35
	s_movk_i32 s0, 3
	s_movk_i32 s2, 24
	s_mov_b32 s4, 0xfc00
	s_mov_b32 s5, 0x15e00
	s_mov_b32 s34, 0x14400
	s_branch .Lmoe_p4
.Lmoe_site_T1:
	s_nop 1
	v_writelane_b32 v255, s0, 0
	v_writelane_b32 v255, s1, 1
	v_writelane_b32 v255, s2, 2
	v_writelane_b32 v255, s3, 3
	v_writelane_b32 v255, s4, 4
	v_writelane_b32 v255, s5, 5
	v_writelane_b32 v255, s6, 6
	v_writelane_b32 v255, s7, 7
	v_writelane_b32 v255, s8, 8
	v_writelane_b32 v255, s9, 9
	v_writelane_b32 v255, s10, 10
	v_writelane_b32 v255, s11, 11
	v_writelane_b32 v255, s12, 12
	v_writelane_b32 v255, s13, 13
	v_writelane_b32 v255, s14, 14
	v_writelane_b32 v255, s15, 15
	v_writelane_b32 v255, s16, 16
	v_writelane_b32 v255, s17, 17
	v_writelane_b32 v255, s18, 18
	v_writelane_b32 v255, s19, 19
	v_writelane_b32 v255, s20, 20
	v_writelane_b32 v255, s21, 21
	v_writelane_b32 v255, s22, 22
	v_writelane_b32 v255, s23, 23
	v_writelane_b32 v255, s24, 24
	v_writelane_b32 v255, s25, 25
	v_writelane_b32 v255, s26, 26
	v_writelane_b32 v255, s27, 27
	v_writelane_b32 v255, s28, 28
	v_writelane_b32 v255, s29, 29
	v_writelane_b32 v255, s30, 30
	v_writelane_b32 v255, s31, 31
	v_writelane_b32 v255, s32, 32
	v_writelane_b32 v255, s33, 33
	v_writelane_b32 v255, s34, 34
	v_writelane_b32 v255, s35, 35
	s_movk_i32 s0, 4
	v_readlane_b32 s20, v252, 32
	s_nop 3
	s_cmp_eq_u32 s20, 0
	s_cbranch_scc1 .Lmoe_T1_l1
	s_movk_i32 s2, 32
	s_movk_i32 s26, 1792
	s_mov_b32 s27, 0x2200
	s_mov_b32 s28, 0x4400
	s_mov_b32 s29, 0x5600
	s_mov_b32 s32, 0xb800
	s_mov_b32 s33, 0x11a00
	s_mov_b32 s5, 0x4600
	s_mov_b32 s35, 0x0
	s_movk_i32 s34, 10
	s_branch .Lmoe_tail
.Lmoe_T1_l1:
	s_movk_i32 s2, 32
	s_movk_i32 s26, 1792
	s_mov_b32 s27, 0x3200
	s_mov_b32 s28, 0x6e00
	s_mov_b32 s29, 0x1c600
	s_mov_b32 s32, 0x20e00
	s_mov_b32 s33, 0x25600
	s_mov_b32 s5, 0xaa00
	s_mov_b32 s35, 0x6400
	s_movk_i32 s34, 10
	s_branch .Lmoe_tail
.Lmoe_site_T2:
	s_nop 1
	v_writelane_b32 v255, s0, 0
	v_writelane_b32 v255, s1, 1
	v_writelane_b32 v255, s2, 2
	v_writelane_b32 v255, s3, 3
	v_writelane_b32 v255, s4, 4
	v_writelane_b32 v255, s5, 5
	v_writelane_b32 v255, s6, 6
	v_writelane_b32 v255, s7, 7
	v_writelane_b32 v255, s8, 8
	v_writelane_b32 v255, s9, 9
	v_writelane_b32 v255, s10, 10
	v_writelane_b32 v255, s11, 11
	v_writelane_b32 v255, s12, 12
	v_writelane_b32 v255, s13, 13
	v_writelane_b32 v255, s14, 14
	v_writelane_b32 v255, s15, 15
	v_writelane_b32 v255, s16, 16
	v_writelane_b32 v255, s17, 17
	v_writelane_b32 v255, s18, 18
	v_writelane_b32 v255, s19, 19
	v_writelane_b32 v255, s20, 20
	v_writelane_b32 v255, s21, 21
	v_writelane_b32 v255, s22, 22
	v_writelane_b32 v255, s23, 23
	v_writelane_b32 v255, s24, 24
	v_writelane_b32 v255, s25, 25
	v_writelane_b32 v255, s26, 26
	v_writelane_b32 v255, s27, 27
	v_writelane_b32 v255, s28, 28
	v_writelane_b32 v255, s29, 29
	v_writelane_b32 v255, s30, 30
	v_writelane_b32 v255, s31, 31
	v_writelane_b32 v255, s32, 32
	v_writelane_b32 v255, s33, 33
	v_writelane_b32 v255, s34, 34
	v_writelane_b32 v255, s35, 35
	s_movk_i32 s0, 5
	v_readlane_b32 s20, v252, 32
	s_nop 3
	s_cmp_eq_u32 s20, 0
	s_cbranch_scc1 .Lmoe_T2_l1
	s_movk_i32 s2, 128
	s_movk_i32 s26, 1024
	s_mov_b32 s27, 0x3200
	s_mov_b32 s28, 0x6e00
	s_mov_b32 s29, 0x1c600
	s_mov_b32 s32, 0x20e00
	s_mov_b32 s33, 0x25600
	s_mov_b32 s5, 0x4000
	s_mov_b32 s35, 0x0
	s_movk_i32 s34, 16
	s_branch .Lmoe_tail

.Lmoe_site_T3:
	s_nop 1
	v_writelane_b32 v255, s0, 0
	v_writelane_b32 v255, s1, 1
	v_writelane_b32 v255, s2, 2
	v_writelane_b32 v255, s3, 3
	v_writelane_b32 v255, s4, 4
	v_writelane_b32 v255, s5, 5
	v_writelane_b32 v255, s6, 6
	v_writelane_b32 v255, s7, 7
	v_writelane_b32 v255, s8, 8
	v_writelane_b32 v255, s9, 9
	v_writelane_b32 v255, s10, 10
	v_writelane_b32 v255, s11, 11
	v_writelane_b32 v255, s12, 12
	v_writelane_b32 v255, s13, 13
	v_writelane_b32 v255, s14, 14
	v_writelane_b32 v255, s15, 15
	v_writelane_b32 v255, s16, 16
	v_writelane_b32 v255, s17, 17
	v_writelane_b32 v255, s18, 18
	v_writelane_b32 v255, s19, 19
	v_writelane_b32 v255, s20, 20
	v_writelane_b32 v255, s21, 21
	v_writelane_b32 v255, s22, 22
	v_writelane_b32 v255, s23, 23
	v_writelane_b32 v255, s24, 24
	v_writelane_b32 v255, s25, 25
	v_writelane_b32 v255, s26, 26
	v_writelane_b32 v255, s27, 27
	v_writelane_b32 v255, s28, 28
	v_writelane_b32 v255, s29, 29
	v_writelane_b32 v255, s30, 30
	v_writelane_b32 v255, s31, 31
	v_writelane_b32 v255, s32, 32
	v_writelane_b32 v255, s33, 33
	v_writelane_b32 v255, s34, 34
	v_writelane_b32 v255, s35, 35
	s_movk_i32 s0, 6
	v_readlane_b32 s20, v252, 32
	s_nop 3
	s_cmp_eq_u32 s20, 0
	s_cbranch_scc1 .Lmoe_T3_l1
	s_movk_i32 s2, 128
	s_movk_i32 s26, 1024
	s_mov_b32 s27, 0x2200
	s_mov_b32 s28, 0x4400
	s_mov_b32 s29, 0x5600
	s_mov_b32 s32, 0xb800
	s_mov_b32 s33, 0x11a00
	s_mov_b32 s5, 0x6600
	s_mov_b32 s35, 0x4600
	s_movk_i32 s34, 8
	s_branch .Lmoe_tail
.Lmoe_T3_l1:
	s_movk_i32 s2, 64
	s_movk_i32 s26, 1536
	s_mov_b32 s27, 0x3200
	s_mov_b32 s28, 0x6e00
	s_mov_b32 s29, 0x1c600
	s_mov_b32 s32, 0x20e00
	s_mov_b32 s33, 0x25600
	s_mov_b32 s5, 0x6400
	s_mov_b32 s35, 0x4000
	s_movk_i32 s34, 6
	s_branch .Lmoe_tail

.LBB0_2493:
	v_mov_b32_e32 v4, s66
	ds_read_b64 v[4:5], v4
	v_mov_b32_e32 v6, v65
	v_mov_b32_e32 v7, v57
	v_mov_b32_e32 v82, v67
	v_mov_b32_e32 v83, v59
	s_waitcnt lgkmcnt(0)
	v_readfirstlane_b32 s2, v4
	v_readfirstlane_b32 s3, v5
	v_mov_b32_e32 v4, v64
	v_mov_b32_e32 v5, v56
	v_pk_mul_f32 v[6:7], v[6:7], v[6:7]
	v_mov_b32_e32 v80, v66
	v_mov_b32_e32 v81, v58
	v_pk_mul_f32 v[82:83], v[82:83], v[82:83]
	v_pk_fma_f32 v[4:5], v[4:5], v[4:5], v[6:7]
	v_pk_fma_f32 v[6:7], v[80:81], v[80:81], v[82:83]
	v_mov_b32_e32 v80, v142
	v_pk_add_f32 v[4:5], v[4:5], v[6:7]
	v_pk_mul_f32 v[6:7], v[50:51], v[50:51]
	v_pk_add_f32 v[4:5], v[4:5], v[4:5] op_sel_hi:[0,1]
	v_mov_b32_e32 v81, v7
	v_pk_mov_b32 v[6:7], v[142:143], v[6:7] op_sel:[1,0]
	v_pk_fma_f32 v[82:83], v[42:43], v[42:43], v[138:139] op_sel_hi:[1,1,0]
	v_pk_add_f32 v[6:7], v[6:7], v[80:81]
	v_pk_fma_f32 v[80:81], v[40:41], v[40:41], v[140:141] op_sel_hi:[1,1,0]
	v_pk_add_f32 v[6:7], v[6:7], v[6:7] op_sel_hi:[0,1]
	v_mov_b32_e32 v129, v81
	v_mov_b32_e32 v133, v83
	v_mov_b32_e32 v125, v7
	v_mov_b32_e32 v127, v5
	v_pk_add_f32 v[80:81], v[128:129], v[132:133]
	v_pk_add_f32 v[4:5], v[124:125], v[126:127]
	v_pk_mul_f32 v[6:7], v[26:27], v[26:27]
	v_pk_add_f32 v[4:5], v[80:81], v[4:5]
	v_mov_b32_e32 v80, v136
	v_mov_b32_e32 v81, v7
	v_pk_mov_b32 v[6:7], v[136:137], v[6:7] op_sel:[1,0]
	s_add_u32 s44, s12, s44
	v_pk_add_f32 v[6:7], v[6:7], v[80:81]
	s_addc_u32 s45, s15, s45
	v_pk_add_f32 v[4:5], v[4:5], v[4:5] op_sel_hi:[0,1]
	v_pk_add_f32 v[6:7], v[6:7], v[6:7] op_sel_hi:[0,1]
	v_pk_fma_f32 v[80:81], v[16:17], v[16:17], v[134:135] op_sel_hi:[1,1,0]
	v_pk_fma_f32 v[82:83], v[18:19], v[18:19], v[130:131] op_sel_hi:[1,1,0]
	s_add_u32 s0, s12, s46
	v_mov_b32_e32 v121, v81
	v_mov_b32_e32 v123, v83
	v_mov_b32_e32 v117, v7
	v_mov_b32_e32 v119, v5
	s_addc_u32 s1, s15, s47
	v_pk_add_f32 v[80:81], v[120:121], v[122:123]
	v_pk_add_f32 v[4:5], v[116:117], v[118:119]
	s_add_u32 s36, s2, 0x2000
	v_pk_add_f32 v[120:121], v[80:81], v[4:5]
	v_and_b32_e32 v5, 64, v207
	s_addc_u32 s37, s3, 0
	v_xor_b32_e32 v4, 16, v207
	v_add_u32_e32 v130, 64, v5
	s_add_u32 s46, s44, 0x2000
	v_cmp_lt_i32_e32 vcc, v4, v130
	s_addc_u32 s47, s45, 0
	v_mov_b32_e32 v124, v61
	v_cndmask_b32_e32 v4, v207, v4, vcc
	v_lshlrev_b32_e32 v131, 2, v4
	s_nop 5
	global_load_dwordx4 v[144:147], v2, s[46:47]
	global_load_dwordx4 v[148:151], v2, s[36:37]
	global_load_dwordx4 v[152:155], v2, s[44:45]
	global_load_dwordx4 v[164:167], v156, s[36:37]
	global_load_dwordx4 v[168:171], v156, s[46:47]
	global_load_dwordx4 v[172:175], v2, s[44:45] offset:1024
	global_load_dwordx4 v[176:179], v157, s[36:37]
	global_load_dwordx4 v[180:183], v157, s[46:47]
	global_load_dwordx4 v[184:187], v2, s[44:45] offset:2048
	global_load_dwordx4 v[190:193], v158, s[36:37]
	global_load_dwordx4 v[212:215], v158, s[46:47]
	global_load_dwordx4 v[216:219], v2, s[44:45] offset:3072
	global_load_dwordx4 v[224:227], v159, s[36:37]
	global_load_dwordx4 v[228:231], v159, s[46:47]
	global_load_dwordx4 v[232:235], v159, s[44:45]
	global_load_dwordx4 v[236:239], v160, s[36:37]
	global_load_dwordx4 v[240:243], v160, s[46:47]
	global_load_dwordx4 v[244:247], v160, s[44:45]
	global_load_dwordx4 v[248:251], v161, s[36:37]
	v_mov_b32_e32 v125, v53
	v_mov_b32_e32 v128, v63
	v_mov_b32_e32 v129, v55
	v_mov_b32_e32 v122, v60
	v_mov_b32_e32 v123, v52
	v_pk_mul_f32 v[124:125], v[124:125], v[124:125]
	v_mov_b32_e32 v126, v62
	v_mov_b32_e32 v127, v54
	v_pk_mul_f32 v[128:129], v[128:129], v[128:129]
	v_pk_fma_f32 v[122:123], v[122:123], v[122:123], v[124:125]
	v_pk_fma_f32 v[124:125], v[126:127], v[126:127], v[128:129]
	v_mov_b32_e32 v126, v114
	v_pk_add_f32 v[122:123], v[122:123], v[124:125]
	v_pk_mul_f32 v[124:125], v[46:47], v[46:47]
	v_pk_add_f32 v[122:123], v[122:123], v[122:123] op_sel_hi:[0,1]
	v_mov_b32_e32 v127, v125
	v_pk_mov_b32 v[114:115], v[114:115], v[124:125] op_sel:[1,0]
	v_pk_fma_f32 v[112:113], v[36:37], v[36:37], v[112:113] op_sel_hi:[1,1,0]
	v_pk_add_f32 v[114:115], v[114:115], v[126:127]
	v_pk_fma_f32 v[110:111], v[38:39], v[38:39], v[110:111] op_sel_hi:[1,1,0]
	v_pk_add_f32 v[114:115], v[114:115], v[114:115] op_sel_hi:[0,1]
	v_mov_b32_e32 v105, v113
	v_mov_b32_e32 v107, v111
	v_mov_b32_e32 v97, v115
	v_mov_b32_e32 v99, v123
	v_pk_add_f32 v[104:105], v[104:105], v[106:107]
	v_pk_add_f32 v[96:97], v[96:97], v[98:99]
	v_pk_mul_f32 v[98:99], v[22:23], v[22:23]
	v_pk_add_f32 v[96:97], v[104:105], v[96:97]
	v_mov_b32_e32 v104, v108
	v_mov_b32_e32 v105, v99
	v_pk_mov_b32 v[98:99], v[108:109], v[98:99] op_sel:[1,0]
	v_pk_add_f32 v[96:97], v[96:97], v[96:97] op_sel_hi:[0,1]
	v_pk_add_f32 v[98:99], v[98:99], v[104:105]
	v_pk_fma_f32 v[102:103], v[12:13], v[12:13], v[102:103] op_sel_hi:[1,1,0]
	v_pk_add_f32 v[98:99], v[98:99], v[98:99] op_sel_hi:[0,1]
	v_pk_fma_f32 v[100:101], v[14:15], v[14:15], v[100:101] op_sel_hi:[1,1,0]
	v_mov_b32_e32 v93, v103
	v_mov_b32_e32 v95, v101
	v_mov_b32_e32 v89, v99
	v_mov_b32_e32 v91, v97
	v_pk_add_f32 v[92:93], v[92:93], v[94:95]
	v_pk_add_f32 v[88:89], v[88:89], v[90:91]
	v_mov_b32_e32 v91, v120
	v_pk_add_f32 v[88:89], v[92:93], v[88:89]
	v_xor_b32_e32 v92, 32, v207
	v_mov_b32_e32 v90, v88
	v_mov_b32_e32 v120, v89
	v_pk_add_f32 v[88:89], v[90:91], v[120:121]
	v_cmp_lt_i32_e32 vcc, v92, v130
	s_mov_b32 s2, 0x3a000000
	v_mov_b32_dpp v91, v89 quad_perm:[1,0,3,2] row_mask:0xf bank_mask:0xf bound_ctrl:1
	v_mov_b32_dpp v90, v88 quad_perm:[1,0,3,2] row_mask:0xf bank_mask:0xf bound_ctrl:1
	v_pk_add_f32 v[88:89], v[88:89], v[90:91]
	v_cndmask_b32_e32 v92, v207, v92, vcc
	v_lshlrev_b32_e32 v92, 2, v92
	v_mov_b32_dpp v91, v89 quad_perm:[2,3,0,1] row_mask:0xf bank_mask:0xf bound_ctrl:1
	v_mov_b32_dpp v90, v88 quad_perm:[2,3,0,1] row_mask:0xf bank_mask:0xf bound_ctrl:1
	v_pk_add_f32 v[88:89], v[88:89], v[90:91]
	s_waitcnt vmcnt(18)
	v_mov_b32_e32 v4, v144
	v_mov_b32_e32 v5, v145
	v_mov_b32_e32 v6, v146
	v_mov_b32_e32 v7, v147
	global_load_dwordx4 v[144:147], v161, s[46:47]
	v_pk_add_f32 v[6:7], v[6:7], 1.0 op_sel_hi:[1,0]
	v_mov_b32_dpp v91, v89 row_half_mirror row_mask:0xf bank_mask:0xf bound_ctrl:1
	v_mov_b32_dpp v90, v88 row_half_mirror row_mask:0xf bank_mask:0xf bound_ctrl:1
	v_pk_add_f32 v[88:89], v[88:89], v[90:91]
	v_pk_add_f32 v[4:5], v[4:5], 1.0 op_sel_hi:[1,0]
	s_nop 0
	v_mov_b32_dpp v91, v89 row_mirror row_mask:0xf bank_mask:0xf bound_ctrl:1
	v_mov_b32_dpp v90, v88 row_mirror row_mask:0xf bank_mask:0xf bound_ctrl:1
	v_pk_add_f32 v[88:89], v[88:89], v[90:91]
	ds_bpermute_b32 v91, v131, v89
	ds_bpermute_b32 v90, v131, v88
	s_waitcnt lgkmcnt(0)
	v_pk_add_f32 v[88:89], v[88:89], v[90:91]
	ds_bpermute_b32 v91, v92, v89
	ds_bpermute_b32 v90, v92, v88
	s_waitcnt lgkmcnt(0)
	v_pk_add_f32 v[88:89], v[88:89], v[90:91]
	s_nop 0
	v_pk_fma_f32 v[88:89], v[88:89], s[2:3], v[188:189] op_sel_hi:[1,0,0]
	s_nop 0
	v_mul_f32_e32 v90, 0x4b800000, v89
	v_cmp_gt_f32_e32 vcc, s11, v89
	s_nop 1
	v_cndmask_b32_e32 v89, v89, v90, vcc
	v_rsq_f32_e32 v89, v89
	v_lshl_add_u64 v[90:91], s[42:43], 1, v[78:79]
	s_add_u32 s42, s0, 0x2000
	s_addc_u32 s43, s1, 0
	v_mul_f32_e32 v92, 0x45800000, v89
	v_cndmask_b32_e32 v92, v89, v92, vcc
	v_pk_mul_f32 v[66:67], v[66:67], v[92:93] op_sel_hi:[1,0]
	v_pk_mul_f32 v[64:65], v[64:65], v[92:93] op_sel_hi:[1,0]
	s_waitcnt vmcnt(18)
	v_mov_b32_e32 v80, v148
	v_mov_b32_e32 v81, v149
	v_mov_b32_e32 v82, v150
	v_mov_b32_e32 v83, v151
	global_load_dwordx4 v[148:151], v161, s[44:45]
	v_pk_mul_f32 v[66:67], v[82:83], v[66:67]
	v_pk_mul_f32 v[64:65], v[80:81], v[64:65]
	s_waitcnt vmcnt(18)
	v_mov_b32_e32 v116, v152
	v_mov_b32_e32 v117, v153
	v_mov_b32_e32 v118, v154
	v_mov_b32_e32 v119, v155
	global_load_dwordx4 v[152:155], v162, s[36:37]
	v_pk_fma_f32 v[6:7], v[6:7], v[66:67], v[118:119]
	v_pk_fma_f32 v[4:5], v[4:5], v[64:65], v[116:117]
	v_pk_mul_f32 v[58:59], v[58:59], v[92:93] op_sel_hi:[1,0]
	v_cvt_pk_bf16_f32 v4, v4, v5
	v_cvt_pk_bf16_f32 v5, v6, v7
	global_store_dwordx2 v[90:91], v[4:5], off
	s_nop 0
	v_pk_mul_f32 v[56:57], v[56:57], v[92:93] op_sel_hi:[1,0]
	v_pk_mul_f32 v[50:51], v[50:51], v[92:93] op_sel_hi:[1,0]
	v_pk_mul_f32 v[48:49], v[48:49], v[92:93] op_sel_hi:[1,0]
	v_pk_mul_f32 v[42:43], v[42:43], v[92:93] op_sel_hi:[1,0]
	v_pk_mul_f32 v[40:41], v[40:41], v[92:93] op_sel_hi:[1,0]
	v_pk_mul_f32 v[34:35], v[34:35], v[92:93] op_sel_hi:[1,0]
	v_pk_mul_f32 v[32:33], v[32:33], v[92:93] op_sel_hi:[1,0]
	v_pk_mul_f32 v[26:27], v[26:27], v[92:93] op_sel_hi:[1,0]
	v_pk_mul_f32 v[24:25], v[24:25], v[92:93] op_sel_hi:[1,0]
	v_pk_mul_f32 v[18:19], v[18:19], v[92:93] op_sel_hi:[1,0]
	v_pk_mul_f32 v[16:17], v[16:17], v[92:93] op_sel_hi:[1,0]
	v_cmp_gt_f32_e32 vcc, s11, v88
	s_waitcnt vmcnt(19)
	v_mov_b32_e32 v4, v164
	v_mov_b32_e32 v5, v165
	v_mov_b32_e32 v6, v166
	v_mov_b32_e32 v7, v167
	s_nop 5
	global_load_dwordx4 v[164:167], v162, s[46:47]
	v_pk_mul_f32 v[4:5], v[4:5], v[56:57]
	v_pk_mul_f32 v[6:7], v[6:7], v[58:59]
	s_waitcnt vmcnt(19)
	v_mov_b32_e32 v64, v168
	v_mov_b32_e32 v65, v169
	v_mov_b32_e32 v66, v170
	v_mov_b32_e32 v67, v171
	global_load_dwordx4 v[168:171], v162, s[44:45]
	v_pk_add_f32 v[56:57], v[66:67], 1.0 op_sel_hi:[1,0]
	v_pk_add_f32 v[58:59], v[64:65], 1.0 op_sel_hi:[1,0]
	s_waitcnt vmcnt(19)
	v_mov_b32_e32 v80, v172
	v_mov_b32_e32 v81, v173
	v_mov_b32_e32 v82, v174
	v_mov_b32_e32 v83, v175
	global_load_dwordx4 v[172:175], v2, s[36:37]
	v_pk_fma_f32 v[6:7], v[56:57], v[6:7], v[82:83]
	v_pk_fma_f32 v[4:5], v[58:59], v[4:5], v[80:81]
	s_nop 0
	v_cvt_pk_bf16_f32 v4, v4, v5
	v_cvt_pk_bf16_f32 v5, v6, v7
	global_store_dwordx2 v[90:91], v[4:5], off offset:512
	s_nop 0
	s_waitcnt vmcnt(20)
	v_mov_b32_e32 v4, v176
	v_mov_b32_e32 v5, v177
	v_mov_b32_e32 v6, v178
	v_mov_b32_e32 v7, v179
	global_load_dwordx4 v[176:179], v2, s[42:43]
	v_pk_mul_f32 v[4:5], v[4:5], v[48:49]
	v_pk_mul_f32 v[6:7], v[6:7], v[50:51]
	s_waitcnt vmcnt(20)
	v_mov_b32_e32 v56, v180
	v_mov_b32_e32 v57, v181
	v_mov_b32_e32 v58, v182
	v_mov_b32_e32 v59, v183
	global_load_dwordx4 v[180:183], v2, s[0:1]
	v_pk_add_f32 v[48:49], v[58:59], 1.0 op_sel_hi:[1,0]
	v_pk_add_f32 v[50:51], v[56:57], 1.0 op_sel_hi:[1,0]
	s_waitcnt vmcnt(20)
	v_mov_b32_e32 v64, v184
	v_mov_b32_e32 v65, v185
	v_mov_b32_e32 v66, v186
	v_mov_b32_e32 v67, v187
	global_load_dwordx4 v[184:187], v156, s[36:37]
	v_pk_fma_f32 v[6:7], v[48:49], v[6:7], v[66:67]
	v_pk_fma_f32 v[4:5], v[50:51], v[4:5], v[64:65]
	s_nop 0
	v_cvt_pk_bf16_f32 v4, v4, v5
	v_cvt_pk_bf16_f32 v5, v6, v7
	global_store_dwordx2 v[90:91], v[4:5], off offset:1024
	s_nop 0
	s_waitcnt vmcnt(21)
	v_mov_b32_e32 v4, v190
	v_mov_b32_e32 v5, v191
	v_mov_b32_e32 v6, v192
	v_mov_b32_e32 v7, v193
	global_load_dwordx4 v[190:193], v156, s[42:43]
	v_pk_mul_f32 v[4:5], v[40:41], v[4:5]
	v_pk_mul_f32 v[6:7], v[42:43], v[6:7]
	s_waitcnt vmcnt(21)
	v_mov_b32_e32 v48, v212
	v_mov_b32_e32 v49, v213
	v_mov_b32_e32 v50, v214
	v_mov_b32_e32 v51, v215
	global_load_dwordx4 v[212:215], v2, s[0:1] offset:1024
	v_pk_add_f32 v[40:41], v[50:51], 1.0 op_sel_hi:[1,0]
	v_pk_add_f32 v[42:43], v[48:49], 1.0 op_sel_hi:[1,0]
	s_waitcnt vmcnt(21)
	v_mov_b32_e32 v56, v216
	v_mov_b32_e32 v57, v217
	v_mov_b32_e32 v58, v218
	v_mov_b32_e32 v59, v219
	global_load_dwordx4 v[216:219], v157, s[36:37]
	v_pk_fma_f32 v[6:7], v[6:7], v[40:41], v[58:59]
	v_pk_fma_f32 v[4:5], v[4:5], v[42:43], v[56:57]
	s_nop 0
	v_cvt_pk_bf16_f32 v4, v4, v5
	v_cvt_pk_bf16_f32 v5, v6, v7
	global_store_dwordx2 v[90:91], v[4:5], off offset:1536
	s_nop 0
	s_waitcnt vmcnt(22)
	v_mov_b32_e32 v4, v224
	v_mov_b32_e32 v5, v225
	v_mov_b32_e32 v6, v226
	v_mov_b32_e32 v7, v227
	global_load_dwordx4 v[224:227], v157, s[42:43]
	v_pk_mul_f32 v[4:5], v[32:33], v[4:5]
	v_pk_mul_f32 v[6:7], v[34:35], v[6:7]
	s_waitcnt vmcnt(22)
	v_mov_b32_e32 v40, v228
	v_mov_b32_e32 v41, v229
	v_mov_b32_e32 v42, v230
	v_mov_b32_e32 v43, v231
	global_load_dwordx4 v[228:231], v2, s[0:1] offset:2048
	v_pk_add_f32 v[32:33], v[42:43], 1.0 op_sel_hi:[1,0]
	v_pk_add_f32 v[34:35], v[40:41], 1.0 op_sel_hi:[1,0]
	s_waitcnt vmcnt(22)
	v_mov_b32_e32 v48, v232
	v_mov_b32_e32 v49, v233
	v_mov_b32_e32 v50, v234
	v_mov_b32_e32 v51, v235
	global_load_dwordx4 v[232:235], v158, s[36:37]
	v_pk_fma_f32 v[6:7], v[6:7], v[32:33], v[50:51]
	v_pk_fma_f32 v[4:5], v[4:5], v[34:35], v[48:49]
	s_nop 0
	v_cvt_pk_bf16_f32 v4, v4, v5
	v_cvt_pk_bf16_f32 v5, v6, v7
	global_store_dwordx2 v[90:91], v[4:5], off offset:2048
	s_nop 0
	s_waitcnt vmcnt(23)
	v_mov_b32_e32 v4, v236
	v_mov_b32_e32 v5, v237
	v_mov_b32_e32 v6, v238
	v_mov_b32_e32 v7, v239
	global_load_dwordx4 v[236:239], v158, s[42:43]
	v_pk_mul_f32 v[4:5], v[24:25], v[4:5]
	v_pk_mul_f32 v[6:7], v[26:27], v[6:7]
	s_waitcnt vmcnt(23)
	v_mov_b32_e32 v32, v240
	v_mov_b32_e32 v33, v241
	v_mov_b32_e32 v34, v242
	v_mov_b32_e32 v35, v243
	global_load_dwordx4 v[240:243], v2, s[0:1] offset:3072
	v_pk_add_f32 v[24:25], v[34:35], 1.0 op_sel_hi:[1,0]
	v_pk_add_f32 v[26:27], v[32:33], 1.0 op_sel_hi:[1,0]
	s_waitcnt vmcnt(23)
	v_mov_b32_e32 v40, v244
	v_mov_b32_e32 v41, v245
	v_mov_b32_e32 v42, v246
	v_mov_b32_e32 v43, v247
	global_load_dwordx4 v[244:247], v159, s[36:37]
	v_pk_fma_f32 v[6:7], v[6:7], v[24:25], v[42:43]
	v_pk_fma_f32 v[4:5], v[4:5], v[26:27], v[40:41]
	s_nop 0
	v_cvt_pk_bf16_f32 v4, v4, v5
	v_cvt_pk_bf16_f32 v5, v6, v7
	global_store_dwordx2 v[90:91], v[4:5], off offset:2560
	s_nop 0
	s_waitcnt vmcnt(24)
	v_mov_b32_e32 v4, v248
	v_mov_b32_e32 v5, v249
	v_mov_b32_e32 v6, v250
	v_mov_b32_e32 v7, v251
	global_load_dwordx4 v[248:251], v159, s[42:43]
	v_pk_mul_f32 v[4:5], v[16:17], v[4:5]
	v_pk_mul_f32 v[6:7], v[18:19], v[6:7]
	s_waitcnt vmcnt(24)
	v_mov_b32_e32 v24, v144
	v_mov_b32_e32 v25, v145
	v_mov_b32_e32 v26, v146
	v_mov_b32_e32 v27, v147
	global_load_dwordx4 v[144:147], v159, s[0:1]
	v_pk_add_f32 v[16:17], v[26:27], 1.0 op_sel_hi:[1,0]
	v_pk_add_f32 v[18:19], v[24:25], 1.0 op_sel_hi:[1,0]
	s_waitcnt vmcnt(24)
	v_mov_b32_e32 v32, v148
	v_mov_b32_e32 v33, v149
	v_mov_b32_e32 v34, v150
	v_mov_b32_e32 v35, v151
	global_load_dwordx4 v[148:151], v160, s[36:37]
	v_pk_fma_f32 v[6:7], v[6:7], v[16:17], v[34:35]
	v_pk_fma_f32 v[4:5], v[4:5], v[18:19], v[32:33]
	v_pk_mul_f32 v[32:33], v[84:85], v[92:93] op_sel_hi:[1,0]
	v_cvt_pk_bf16_f32 v4, v4, v5
	v_cvt_pk_bf16_f32 v5, v6, v7
	global_store_dwordx2 v[90:91], v[4:5], off offset:3072
	s_nop 0
	v_pk_mul_f32 v[34:35], v[86:87], v[92:93] op_sel_hi:[1,0]
	s_waitcnt vmcnt(25)
	v_mov_b32_e32 v4, v152
	v_mov_b32_e32 v5, v153
	v_mov_b32_e32 v6, v154
	v_mov_b32_e32 v7, v155
	global_load_dwordx4 v[152:155], v160, s[42:43]
	v_pk_mul_f32 v[6:7], v[32:33], v[6:7]
	v_pk_mul_f32 v[4:5], v[34:35], v[4:5]
	s_waitcnt vmcnt(24)
	v_mov_b32_e32 v16, v164
	v_mov_b32_e32 v17, v165
	v_mov_b32_e32 v18, v166
	v_mov_b32_e32 v19, v167
	global_load_dwordx4 v[164:167], v160, s[0:1]
	v_pk_add_f32 v[18:19], v[18:19], 1.0 op_sel_hi:[1,0]
	v_pk_add_f32 v[16:17], v[16:17], 1.0 op_sel_hi:[1,0]
	s_waitcnt vmcnt(24)
	v_mov_b32_e32 v24, v168
	v_mov_b32_e32 v25, v169
	v_mov_b32_e32 v26, v170
	v_mov_b32_e32 v27, v171
	global_load_dwordx4 v[168:171], v161, s[36:37]
	v_pk_fma_f32 v[6:7], v[6:7], v[18:19], v[26:27]
	v_pk_fma_f32 v[4:5], v[4:5], v[16:17], v[24:25]
	v_mul_f32_e32 v32, 0x4b800000, v88
	v_cvt_pk_bf16_f32 v4, v4, v5
	v_cvt_pk_bf16_f32 v5, v6, v7
	global_store_dwordx2 v[90:91], v[4:5], off offset:3584
	s_nop 0
	v_cndmask_b32_e32 v32, v88, v32, vcc
	v_rsq_f32_e32 v34, v32
	v_lshl_add_u64 v[32:33], s[40:41], 1, v[78:79]
	v_mul_f32_e32 v35, 0x45800000, v34
	v_cndmask_b32_e32 v34, v34, v35, vcc
	v_pk_mul_f32 v[40:41], v[62:63], v[34:35] op_sel_hi:[1,0]
	v_pk_mul_f32 v[42:43], v[60:61], v[34:35] op_sel_hi:[1,0]
	v_pk_mul_f32 v[38:39], v[38:39], v[34:35] op_sel_hi:[1,0]
	v_pk_mul_f32 v[36:37], v[36:37], v[34:35] op_sel_hi:[1,0]
	v_pk_mul_f32 v[30:31], v[30:31], v[34:35] op_sel_hi:[1,0]
	v_pk_mul_f32 v[28:29], v[28:29], v[34:35] op_sel_hi:[1,0]
	v_pk_mul_f32 v[22:23], v[22:23], v[34:35] op_sel_hi:[1,0]
	v_pk_mul_f32 v[20:21], v[20:21], v[34:35] op_sel_hi:[1,0]
	v_pk_mul_f32 v[14:15], v[14:15], v[34:35] op_sel_hi:[1,0]
	v_pk_mul_f32 v[12:13], v[12:13], v[34:35] op_sel_hi:[1,0]
	v_pk_mul_f32 v[10:11], v[10:11], v[34:35] op_sel_hi:[1,0]
	v_pk_mul_f32 v[8:9], v[8:9], v[34:35] op_sel_hi:[1,0]
	s_waitcnt vmcnt(25)
	v_mov_b32_e32 v4, v172
	v_mov_b32_e32 v5, v173
	v_mov_b32_e32 v6, v174
	v_mov_b32_e32 v7, v175
	global_load_dwordx4 v[172:175], v161, s[42:43]
	v_pk_mul_f32 v[4:5], v[4:5], v[42:43]
	v_pk_mul_f32 v[6:7], v[6:7], v[40:41]
	s_waitcnt vmcnt(24)
	v_mov_b32_e32 v16, v176
	v_mov_b32_e32 v17, v177
	v_mov_b32_e32 v18, v178
	v_mov_b32_e32 v19, v179
	global_load_dwordx4 v[176:179], v161, s[0:1]
	v_pk_add_f32 v[18:19], v[18:19], 1.0 op_sel_hi:[1,0]
	v_pk_add_f32 v[16:17], v[16:17], 1.0 op_sel_hi:[1,0]
	s_waitcnt vmcnt(24)
	v_mov_b32_e32 v24, v180
	v_mov_b32_e32 v25, v181
	v_mov_b32_e32 v26, v182
	v_mov_b32_e32 v27, v183
	global_load_dwordx4 v[180:183], v162, s[36:37]
	v_pk_fma_f32 v[6:7], v[18:19], v[6:7], v[26:27]
	v_pk_fma_f32 v[4:5], v[16:17], v[4:5], v[24:25]
	v_pk_mul_f32 v[40:41], v[54:55], v[34:35] op_sel_hi:[1,0]
	v_cvt_pk_bf16_f32 v4, v4, v5
	v_cvt_pk_bf16_f32 v5, v6, v7
	global_store_dwordx2 v[32:33], v[4:5], off
	s_nop 0
	v_pk_mul_f32 v[42:43], v[52:53], v[34:35] op_sel_hi:[1,0]
	s_waitcnt vmcnt(25)
	v_mov_b32_e32 v4, v184
	v_mov_b32_e32 v5, v185
	v_mov_b32_e32 v6, v186
	v_mov_b32_e32 v7, v187
	global_load_dwordx4 v[184:187], v162, s[42:43]
	v_pk_mul_f32 v[6:7], v[6:7], v[40:41]
	v_pk_mul_f32 v[4:5], v[4:5], v[42:43]
	s_waitcnt vmcnt(24)
	v_mov_b32_e32 v16, v190
	v_mov_b32_e32 v17, v191
	v_mov_b32_e32 v18, v192
	v_mov_b32_e32 v19, v193
	global_load_dwordx4 v[190:193], v162, s[0:1]
	v_pk_add_f32 v[18:19], v[18:19], 1.0 op_sel_hi:[1,0]
	v_pk_add_f32 v[16:17], v[16:17], 1.0 op_sel_hi:[1,0]
	s_waitcnt vmcnt(24)
	v_mov_b32_e32 v24, v212
	v_mov_b32_e32 v25, v213
	v_mov_b32_e32 v26, v214
	v_mov_b32_e32 v27, v215
	v_pk_fma_f32 v[6:7], v[18:19], v[6:7], v[26:27]
	v_pk_fma_f32 v[4:5], v[16:17], v[4:5], v[24:25]
	v_pk_mul_f32 v[40:41], v[46:47], v[34:35] op_sel_hi:[1,0]
	v_cvt_pk_bf16_f32 v4, v4, v5
	v_cvt_pk_bf16_f32 v5, v6, v7
	global_store_dwordx2 v[32:33], v[4:5], off offset:512
	s_nop 0
	v_pk_mul_f32 v[42:43], v[44:45], v[34:35] op_sel_hi:[1,0]
	s_waitcnt vmcnt(24)
	v_mov_b32_e32 v4, v216
	v_mov_b32_e32 v5, v217
	v_mov_b32_e32 v6, v218
	v_mov_b32_e32 v7, v219
	v_pk_mul_f32 v[6:7], v[6:7], v[40:41]
	v_pk_mul_f32 v[4:5], v[4:5], v[42:43]
	s_waitcnt vmcnt(22)
	v_mov_b32_e32 v16, v224
	v_mov_b32_e32 v17, v225
	v_mov_b32_e32 v18, v226
	v_mov_b32_e32 v19, v227
	v_pk_add_f32 v[18:19], v[18:19], 1.0 op_sel_hi:[1,0]
	v_pk_add_f32 v[16:17], v[16:17], 1.0 op_sel_hi:[1,0]
	s_waitcnt vmcnt(21)
	v_mov_b32_e32 v24, v228
	v_mov_b32_e32 v25, v229
	v_mov_b32_e32 v26, v230
	v_mov_b32_e32 v27, v231
	v_pk_fma_f32 v[6:7], v[18:19], v[6:7], v[26:27]
	v_pk_fma_f32 v[4:5], v[16:17], v[4:5], v[24:25]
	s_nop 0
	v_cvt_pk_bf16_f32 v4, v4, v5
	v_cvt_pk_bf16_f32 v5, v6, v7
	global_store_dwordx2 v[32:33], v[4:5], off offset:1024
	s_nop 0
	s_waitcnt vmcnt(21)
	v_mov_b32_e32 v4, v232
	v_mov_b32_e32 v5, v233
	v_mov_b32_e32 v6, v234
	v_mov_b32_e32 v7, v235
	v_pk_mul_f32 v[4:5], v[4:5], v[36:37]
	v_pk_mul_f32 v[6:7], v[6:7], v[38:39]
	s_waitcnt vmcnt(19)
	v_mov_b32_e32 v16, v236
	v_mov_b32_e32 v17, v237
	v_mov_b32_e32 v18, v238
	v_mov_b32_e32 v19, v239
	v_pk_add_f32 v[18:19], v[18:19], 1.0 op_sel_hi:[1,0]
	v_pk_add_f32 v[16:17], v[16:17], 1.0 op_sel_hi:[1,0]
	s_waitcnt vmcnt(18)
	v_mov_b32_e32 v24, v240
	v_mov_b32_e32 v25, v241
	v_mov_b32_e32 v26, v242
	v_mov_b32_e32 v27, v243
	v_pk_fma_f32 v[6:7], v[6:7], v[18:19], v[26:27]
	v_pk_fma_f32 v[4:5], v[4:5], v[16:17], v[24:25]
	s_nop 0
	v_cvt_pk_bf16_f32 v4, v4, v5
	v_cvt_pk_bf16_f32 v5, v6, v7
	global_store_dwordx2 v[32:33], v[4:5], off offset:1536
	s_nop 0
	s_waitcnt vmcnt(18)
	v_mov_b32_e32 v4, v244
	v_mov_b32_e32 v5, v245
	v_mov_b32_e32 v6, v246
	v_mov_b32_e32 v7, v247
	v_pk_mul_f32 v[4:5], v[28:29], v[4:5]
	v_pk_mul_f32 v[6:7], v[30:31], v[6:7]
	s_waitcnt vmcnt(16)
	v_mov_b32_e32 v16, v248
	v_mov_b32_e32 v17, v249
	v_mov_b32_e32 v18, v250
	v_mov_b32_e32 v19, v251
	v_pk_add_f32 v[18:19], v[18:19], 1.0 op_sel_hi:[1,0]
	v_pk_add_f32 v[16:17], v[16:17], 1.0 op_sel_hi:[1,0]
	s_waitcnt vmcnt(15)
	v_mov_b32_e32 v24, v144
	v_mov_b32_e32 v25, v145
	v_mov_b32_e32 v26, v146
	v_mov_b32_e32 v27, v147
	v_pk_fma_f32 v[6:7], v[6:7], v[18:19], v[26:27]
	v_pk_fma_f32 v[4:5], v[4:5], v[16:17], v[24:25]
	s_nop 0
	v_cvt_pk_bf16_f32 v4, v4, v5
	v_cvt_pk_bf16_f32 v5, v6, v7
	global_store_dwordx2 v[32:33], v[4:5], off offset:2048
	s_nop 0
	s_waitcnt vmcnt(15)
	v_mov_b32_e32 v4, v148
	v_mov_b32_e32 v5, v149
	v_mov_b32_e32 v6, v150
	v_mov_b32_e32 v7, v151
	v_pk_mul_f32 v[4:5], v[20:21], v[4:5]
	v_pk_mul_f32 v[6:7], v[22:23], v[6:7]
	s_waitcnt vmcnt(13)
	v_mov_b32_e32 v16, v152
	v_mov_b32_e32 v17, v153
	v_mov_b32_e32 v18, v154
	v_mov_b32_e32 v19, v155
	v_pk_add_f32 v[18:19], v[18:19], 1.0 op_sel_hi:[1,0]
	v_pk_add_f32 v[16:17], v[16:17], 1.0 op_sel_hi:[1,0]
	s_waitcnt vmcnt(12)
	v_mov_b32_e32 v24, v164
	v_mov_b32_e32 v25, v165
	v_mov_b32_e32 v26, v166
	v_mov_b32_e32 v27, v167
	v_pk_fma_f32 v[6:7], v[6:7], v[18:19], v[26:27]
	v_pk_fma_f32 v[4:5], v[4:5], v[16:17], v[24:25]
	s_nop 0
	v_cvt_pk_bf16_f32 v4, v4, v5
	v_cvt_pk_bf16_f32 v5, v6, v7
	global_store_dwordx2 v[32:33], v[4:5], off offset:2560
	s_nop 0
	s_waitcnt vmcnt(12)
	v_mov_b32_e32 v4, v168
	v_mov_b32_e32 v5, v169
	v_mov_b32_e32 v6, v170
	v_mov_b32_e32 v7, v171
	v_pk_mul_f32 v[4:5], v[12:13], v[4:5]
	v_pk_mul_f32 v[6:7], v[14:15], v[6:7]
	s_waitcnt vmcnt(10)
	v_mov_b32_e32 v16, v172
	v_mov_b32_e32 v17, v173
	v_mov_b32_e32 v18, v174
	v_mov_b32_e32 v19, v175
	v_pk_add_f32 v[12:13], v[18:19], 1.0 op_sel_hi:[1,0]
	v_pk_add_f32 v[14:15], v[16:17], 1.0 op_sel_hi:[1,0]
	s_waitcnt vmcnt(9)
	v_mov_b32_e32 v20, v176
	v_mov_b32_e32 v21, v177
	v_mov_b32_e32 v22, v178
	v_mov_b32_e32 v23, v179
	v_pk_fma_f32 v[6:7], v[6:7], v[12:13], v[22:23]
	v_pk_fma_f32 v[4:5], v[4:5], v[14:15], v[20:21]
	s_nop 0
	v_cvt_pk_bf16_f32 v4, v4, v5
	v_cvt_pk_bf16_f32 v5, v6, v7
	global_store_dwordx2 v[32:33], v[4:5], off offset:3072
	s_nop 0
	s_waitcnt vmcnt(9)
	v_mov_b32_e32 v4, v180
	v_mov_b32_e32 v5, v181
	v_mov_b32_e32 v6, v182
	v_mov_b32_e32 v7, v183
	v_pk_mul_f32 v[4:5], v[8:9], v[4:5]
	v_pk_mul_f32 v[6:7], v[10:11], v[6:7]
	s_waitcnt vmcnt(7)
	v_mov_b32_e32 v12, v184
	v_mov_b32_e32 v13, v185
	v_mov_b32_e32 v14, v186
	v_mov_b32_e32 v15, v187
	v_pk_add_f32 v[8:9], v[14:15], 1.0 op_sel_hi:[1,0]
	v_pk_add_f32 v[10:11], v[12:13], 1.0 op_sel_hi:[1,0]
	s_waitcnt vmcnt(6)
	v_mov_b32_e32 v16, v190
	v_mov_b32_e32 v17, v191
	v_mov_b32_e32 v18, v192
	v_mov_b32_e32 v19, v193
	v_pk_fma_f32 v[6:7], v[6:7], v[8:9], v[18:19]
	v_pk_fma_f32 v[4:5], v[4:5], v[10:11], v[16:17]
	s_nop 0
	v_cvt_pk_bf16_f32 v4, v4, v5
	v_cvt_pk_bf16_f32 v5, v6, v7
	global_store_dwordx2 v[32:33], v[4:5], off offset:3584
